# P9 prologue: the first unit's four rowtok gathers issued back to back (one wait instead of four)
# baseline (speedup 1.0000x reference)
.LBB0_1335:
	v_mov_b32_e32 v230, 0
	v_mov_b32_e32 v231, 0
	v_mov_b32_e32 v232, 0
	v_mov_b32_e32 v233, 0
	s_andn2_b64 vcc, exec, s[4:5]
	s_cbranch_vccnz .LBB0_1374
	v_ashrrev_i32_e32 v1, 31, v6
	v_lshrrev_b32_e32 v1, 26, v1
	v_add_u32_e32 v1, v6, v1
	v_ashrrev_i32_e32 v8, 6, v1
	v_bfe_i32 v1, v6, 27, 1
	v_lshlrev_b32_e32 v10, 4, v6
	v_lshrrev_b32_e32 v1, 22, v1
	v_add_u32_e32 v1, v10, v1
	s_add_u32 s25, s6, 0x5f30000
	v_and_b32_e32 v1, 0xfffffc00, v1
	s_addc_u32 s56, s7, 0
	v_sub_u32_e32 v1, v10, v1
	s_lshl_b32 s2, s36, 2
	v_lshrrev_b32_e32 v2, 4, v1
	s_add_i32 s2, s2, 0
	v_bitop3_b32 v9, v2, v1, 32 bitop3:0x6c
	v_lshlrev_b32_e32 v2, 3, v8
	s_add_i32 s2, s2, 0x21040
	v_and_b32_e32 v4, -16, v2
	v_mov_b32_e32 v2, s2
	ds_read2st64_b32 v[2:3], v2 offset1:1
	v_ashrrev_i32_e32 v1, 31, v1
	v_lshrrev_b32_e32 v1, 26, v1
	v_add_u32_e32 v1, v9, v1
	v_ashrrev_i32_e32 v7, 6, v1
	s_ashr_i32 s37, s36, 31
	s_waitcnt lgkmcnt(0)
	v_sub_u32_e32 v2, s23, v2
	v_add_u32_e32 v1, v7, v4
	v_lshlrev_b32_e32 v2, 8, v2
	s_lshl_b64 s[2:3], s[36:37], 16
	s_add_u32 s2, s25, s2
	v_add_u32_e32 v4, v2, v1
	s_addc_u32 s3, s56, s3
	v_cmp_lt_i32_e32 vcc, v4, v3
	v_mov_b32_e32 v12, 0
	v_mov_b32_e32 v11, 0
	s_and_saveexec_b64 s[4:5], vcc
	s_cbranch_execz .LBB0_1338
	v_ashrrev_i32_e32 v5, 31, v4
	v_lshl_add_u64 v[4:5], v[4:5], 2, s[2:3]
	global_load_dword v230, v[4:5], off
.LBB0_1338:
	s_or_b64 exec, exec, s[4:5]
	v_add_u32_e32 v4, 0x2000, v10
	v_ashrrev_i32_e32 v5, 31, v4
	v_lshrrev_b32_e32 v5, 22, v5
	v_add_u32_e32 v5, v4, v5
	v_ashrrev_i32_e32 v13, 10, v5
	v_mul_i32_i24_e32 v5, 0x400, v13
	v_sub_u32_e32 v4, v4, v5
	v_lshrrev_b32_e32 v5, 4, v4
	v_bitop3_b32 v15, v5, v4, 32 bitop3:0x6c
	v_ashrrev_i32_e32 v5, 31, v15
	v_lshrrev_b32_e32 v5, 26, v5
	v_lshlrev_b32_e32 v4, 3, v13
	v_add_u32_e32 v5, v15, v5
	v_and_b32_e32 v4, -16, v4
	v_ashrrev_i32_e32 v10, 6, v5
	v_add_u32_e32 v182, v10, v4
	v_add_u32_e32 v4, v2, v182
	v_cmp_lt_i32_e32 vcc, v4, v3
	s_and_saveexec_b64 s[4:5], vcc
	s_cbranch_execz .LBB0_1340
	v_ashrrev_i32_e32 v5, 31, v4
	v_lshl_add_u64 v[4:5], v[4:5], 2, s[2:3]
	global_load_dword v231, v[4:5], off
.LBB0_1340:
	s_or_b64 exec, exec, s[4:5]
	v_or_b32_e32 v2, 0x80, v2
	v_add_u32_e32 v4, v2, v1
	v_cmp_lt_i32_e32 vcc, v4, v3
	v_mov_b32_e32 v14, 0
	v_mov_b32_e32 v5, 0
	s_and_saveexec_b64 s[4:5], vcc
	s_cbranch_execz .LBB0_1342
	v_ashrrev_i32_e32 v5, 31, v4
	v_lshl_add_u64 v[4:5], v[4:5], 2, s[2:3]
	global_load_dword v232, v[4:5], off
.LBB0_1342:
	s_or_b64 exec, exec, s[4:5]
	v_add_u32_e32 v2, v2, v182
	v_cmp_lt_i32_e32 vcc, v2, v3
	s_and_saveexec_b64 s[4:5], vcc
	s_cbranch_execz .LBB0_1344
	v_ashrrev_i32_e32 v3, 31, v2
	v_lshl_add_u64 v[2:3], v[2:3], 2, s[2:3]
	global_load_dword v233, v[2:3], off
.LBB0_1344:
	s_or_b64 exec, exec, s[4:5]
	s_waitcnt vmcnt(0)
	v_lshlrev_b32_e32 v11, 11, v230
	v_lshlrev_b32_e32 v12, 11, v231
	v_lshlrev_b32_e32 v5, 11, v232
	v_lshlrev_b32_e32 v14, 11, v233
	v_mul_i32_i24_e32 v3, 64, v7
	v_sub_u32_e32 v3, v9, v3
	v_mov_b32_e32 v4, 1
	v_lshlrev_b32_e32 v2, 5, v8
	v_ashrrev_i16_sdwa v3, v4, sext(v3) dst_sel:DWORD dst_unused:UNUSED_PAD src0_sel:DWORD src1_sel:BYTE_0
	v_and_b32_e32 v2, 32, v2
	v_bfe_i32 v3, v3, 0, 16
	v_add_lshl_u32 v183, v2, v3, 1
	v_lshlrev_b32_e32 v3, 6, v10
	v_sub_u32_e32 v3, v15, v3
	v_lshlrev_b32_e32 v2, 5, v13
	v_ashrrev_i16_sdwa v3, v4, sext(v3) dst_sel:DWORD dst_unused:UNUSED_PAD src0_sel:DWORD src1_sel:BYTE_0
	s_ashr_i32 s35, s34, 31
	v_and_b32_e32 v2, 32, v2
	v_bfe_i32 v3, v3, 0, 16
	s_lshl_b64 s[12:13], s[36:37], 23
	s_lshl_b64 s[14:15], s[34:35], 19
	v_add_lshl_u32 v184, v2, v3, 1
	s_add_u32 s2, s6, 0x2e000000
	v_lshlrev_b32_e32 v2, 1, v1
	v_lshrrev_b32_e32 v3, 2, v1
	v_and_b32_e32 v4, 3, v7
	s_mov_b32 s5, 0x1fffe0
	s_addc_u32 s3, s7, 0
	v_and_b32_e32 v2, 24, v2
	v_and_b32_e32 v3, 4, v3
	v_and_or_b32 v4, v1, s5, v4
	s_add_u32 s35, s6, 0x56000000
	v_or3_b32 v2, v4, v3, v2
	v_and_b32_e32 v4, 3, v10
	s_addc_u32 s57, s7, 0
	v_and_or_b32 v4, v182, s5, v4
	s_ashr_i32 s5, s18, 6
	s_ashr_i32 s4, s18, 8
	s_lshl_b32 s58, s5, 10
	s_add_u32 s12, s35, s12
	s_addc_u32 s13, s57, s13
	s_add_u32 s38, s12, s14
	v_lshl_add_u32 v164, v2, 11, v183
	v_lshlrev_b32_e32 v2, 1, v182
	v_lshrrev_b32_e32 v3, 2, v182
	s_addc_u32 s39, s13, s15
	s_add_i32 s59, s58, 0
	v_and_b32_e32 v2, 24, v2
	v_and_b32_e32 v3, 4, v3
	s_add_i32 m0, s59, 0x10000
	v_or3_b32 v2, v4, v3, v2
	global_load_lds_dwordx4 v164, s[38:39]
	s_add_i32 m0, s59, 0x12000
	v_lshl_add_u32 v166, v2, 11, v184
	s_add_u32 s12, s38, 0x40000
	global_load_lds_dwordx4 v166, s[38:39]
	s_addc_u32 s13, s39, 0
	s_add_i32 m0, s59, 0x14000
	v_add_u32_e32 v162, v11, v183
	global_load_lds_dwordx4 v164, s[12:13]
	s_add_i32 m0, s59, 0x16000
	s_add_i32 s60, s59, 0x2000
	global_load_lds_dwordx4 v166, s[12:13]
	s_mov_b32 m0, s59
	v_add_u32_e32 v170, v12, v184
	global_load_lds_dwordx4 v162, s[2:3]
	s_mov_b32 m0, s60
	s_add_i32 s61, s59, 0x4000
	v_add_u32_e32 v168, v5, v183
	global_load_lds_dwordx4 v170, s[2:3]
	s_mov_b32 m0, s61
	s_add_i32 s62, s59, 0x6000
	v_add_u32_e32 v172, v14, v184
	global_load_lds_dwordx4 v168, s[2:3]
	s_mov_b32 m0, s62
	s_load_dwordx2 s[10:11], s[10:11], 0xd8
	global_load_lds_dwordx4 v172, s[2:3]
	v_mov_b32_e32 v163, 0
	v_mov_b32_e32 v165, v163
	v_mov_b32_e32 v167, v163
	s_cmp_eq_u32 s4, 1
	v_lshl_add_u64 v[4:5], s[38:39], 0, v[164:165]
	s_mov_b32 s63, 0
	v_lshl_add_u64 v[2:3], s[38:39], 0, v[166:167]
	s_cselect_b64 s[12:13], -1, 0
	s_cmp_lg_u32 s4, 1
	v_mov_b32_e32 v171, v163
	s_cbranch_scc1 .LBB0_1346
	s_barrier
